# routed-expert item setup: first-group row-list entries requested together with the expert's row count (masked after the count arrives); one round trip less per gate/up and down item
# speedup vs baseline: 1.0368x; 1.0017x over previous
.LBB0_1291:
	s_or_b64 exec, exec, s[0:1]
	v_readlane_b32 s0, v254, 54
	s_waitcnt lgkmcnt(0)
	s_barrier
	v_mov_b32_e32 v0, s0
	ds_read_b32 v0, v0
	s_movk_i32 s0, 0x4ff
	s_waitcnt lgkmcnt(0)
	v_cmp_lt_i32_e32 vcc, s0, v0
	v_readfirstlane_b32 s66, v0
	s_mov_b64 s[0:1], -1
	s_cbranch_vccnz .LBB0_1282
	s_add_i32 s0, s66, 0xffffff00
	s_ashr_i32 s2, s0, 2
	s_cmpk_gt_i32 s66, 0xff
	s_cselect_b64 s[68:69], -1, 0
	s_and_b64 s[0:1], s[68:69], exec
	s_cselect_b32 s0, s2, s66
	s_lshl_b32 s8, s0, 5
	s_ashr_i32 s9, s8, 31
	s_lshl_b64 s[8:9], s[8:9], 2
	s_add_u32 s8, s50, s8
	s_addc_u32 s9, s51, s9
	global_load_dword v0, v1, s[8:9]
	s_ashr_i32 s1, s0, 31
	s_lshl_b64 s[36:37], s[0:1], 16
	v_readlane_b32 s38, v255, 15
	v_readlane_b32 s39, v255, 16
	s_add_u32 s36, s38, s36
	s_addc_u32 s37, s39, s37
	v_lshlrev_b32_e32 v218, 2, v231
	global_load_dword v219, v218, s[36:37]
	global_load_dword v218, v218, s[36:37] offset:2048
	s_waitcnt vmcnt(0)
	v_cmp_gt_i32_e32 vcc, 1, v0
	v_readfirstlane_b32 s84, v0
	s_cbranch_vccnz .LBB0_1281
	s_max_i32 s1, s66, 0x100
	s_and_b32 s27, s1, 3
	s_and_b64 s[8:9], s[68:69], exec
	s_cselect_b32 s2, 1, 4
	s_ashr_i32 s1, s0, 31
	s_lshl_b64 s[8:9], s[0:1], 16
	v_readlane_b32 s11, v255, 15
	s_add_u32 s70, s11, s8
	v_readlane_b32 s8, v255, 16
	s_addc_u32 s71, s8, s9
	s_ashr_i32 s67, s66, 31
	s_and_b32 s11, s66, 3
	s_lshl_b64 s[8:9], s[66:67], 20
	v_readlane_b32 s14, v255, 19
	s_add_u32 s67, s14, s8
	v_readlane_b32 s15, v255, 20
	s_addc_u32 s38, s15, s9
	s_add_i32 s8, s27, s11
	s_lshl_b32 s8, s8, 8
	s_add_u32 s34, s67, s8
	s_addc_u32 s35, s38, 0
	s_add_u32 s36, s34, 0x4000
	s_addc_u32 s37, s35, 0
	s_add_u32 s96, s34, 0x10000
	s_addc_u32 s97, s35, 0
	s_add_u32 s92, s96, 0x4000
	s_addc_u32 s93, s97, 0
	s_add_u32 s88, s34, 0x20000
	s_addc_u32 s89, s35, 0
	s_add_u32 s8, s88, 0x4000
	s_addc_u32 s9, s89, 0
	s_add_i32 s77, s2, -1
	s_and_b32 s76, s0, s77
	s_lshl_b64 s[0:1], s[0:1], 20
	s_lshl_b32 s40, s2, 4
	s_and_b64 s[12:13], s[68:69], exec
	s_cselect_b32 s2, 0x800, 0
	v_readlane_b32 s11, v255, 7
	s_add_i32 s41, s11, s2
	s_add_u32 s11, s14, s0
	s_addc_u32 s79, s15, s1
	s_add_i32 s0, s76, s27
	s_lshl_b32 s0, s0, 8
	s_add_u32 s30, s11, s0
	s_addc_u32 s31, s79, 0
	s_add_u32 s94, s30, 0x4000
	s_addc_u32 s95, s31, 0
	s_add_u32 s12, s30, 0x10000
	s_addc_u32 s13, s31, 0
	s_add_u32 s14, s12, 0x4000
	s_addc_u32 s15, s13, 0
	s_add_u32 s16, s30, 0x20000
	s_addc_u32 s17, s31, 0
	s_add_u32 s18, s16, 0x4000
	s_addc_u32 s19, s17, 0
	s_and_b64 s[0:1], s[68:69], exec
	s_cselect_b32 s82, 0x200, 0
	s_lshl_b32 s0, s82, 2
	s_mov_b32 s48, 0
	s_add_i32 s86, s87, s0
	s_branch .LBB0_1297

.LBB0_1297:
	s_sub_i32 s29, s84, s48
	s_cmpk_lt_i32 s29, 0x241
	s_cselect_b64 s[0:1], -1, 0
	s_and_b64 s[42:43], s[68:69], s[0:1]
	s_mov_b64 s[0:1], -1
	s_and_b64 vcc, exec, s[42:43]
	s_cbranch_vccnz .LBB0_1296
	s_cmp_lg_u32 s48, 0
	s_cbranch_scc1 .Lgf_slow
	v_mov_b32_e32 v2, 0x24000
	v_cmp_gt_i32_e32 vcc, s84, v231
	v_add_u32_e32 v4, 0x200, v231
	s_nop 0
	v_cndmask_b32_e32 v3, v2, v219, vcc
	v_cmp_gt_i32_e32 vcc, s84, v4
	s_mov_b64 s[0:1], exec
	s_nop 0
	v_cndmask_b32_e32 v0, v2, v218, vcc
	v_mov_b32_e32 v2, v231
	s_branch .LBB0_1302
.Lgf_slow:
	s_waitcnt vmcnt(9)
	v_mov_b32_e32 v4, v231
	v_mov_b32_e32 v0, 0x24000
	v_add_u32_e32 v2, s48, v4
	v_cmp_gt_i32_e32 vcc, s84, v2
	v_mov_b32_e32 v3, 0x24000
	s_and_saveexec_b64 s[0:1], vcc
	s_cbranch_execz .LBB0_1300
	v_ashrrev_i32_e32 v3, 31, v2
	v_lshl_add_u64 v[2:3], v[2:3], 2, s[70:71]
	global_load_dword v3, v[2:3], off

.LBB0_1414:
	s_or_b64 exec, exec, s[36:37]
	v_readlane_b32 s25, v254, 54
	s_waitcnt lgkmcnt(0)
	s_barrier
	v_mov_b32_e32 v0, s25
	ds_read_b32 v0, v0
	s_movk_i32 s36, 0x4ff
	s_waitcnt lgkmcnt(0)
	v_cmp_lt_i32_e32 vcc, s36, v0
	v_readfirstlane_b32 s25, v0
	s_mov_b64 s[36:37], -1
	s_cbranch_vccnz .LBB0_1405
	s_add_i32 s36, s25, 0xffffff00
	s_ashr_i32 s44, s36, 2
	s_cmpk_gt_i32 s25, 0xff
	s_cselect_b64 s[36:37], -1, 0
	s_and_b64 s[42:43], s[36:37], exec
	s_cselect_b32 s42, s44, s25
	s_lshl_b32 s44, s42, 5
	s_ashr_i32 s45, s44, 31
	s_lshl_b64 s[44:45], s[44:45], 2
	s_add_u32 s44, s0, s44
	s_addc_u32 s45, s1, s45
	global_load_dword v0, v1, s[44:45]
	s_ashr_i32 s43, s42, 31
	s_lshl_b64 s[46:47], s[42:43], 16
	s_add_u32 s46, s11, s46
	s_addc_u32 s47, s26, s47
	v_lshlrev_b32_e32 v216, 2, v231
	global_load_dword v217, v216, s[46:47] offset:2048
	global_load_dword v216, v216, s[46:47]
	s_waitcnt vmcnt(0)
	v_cmp_gt_i32_e32 vcc, 1, v0
	v_readfirstlane_b32 s76, v0
	s_cbranch_vccnz .LBB0_1404
	s_lshl_b32 s25, s25, 1
	s_and_b32 s25, s25, 6
	s_and_b64 s[46:47], s[36:37], exec
	s_cselect_b32 s77, s25, 0
	s_cselect_b32 s25, 2, 8
	s_ashr_i32 s43, s42, 31
	s_lshl_b64 s[46:47], s[42:43], 16
	s_add_u32 s46, s11, s46
	s_addc_u32 s47, s26, s47
	s_add_i32 s78, s25, -1
	s_lshl_b64 s[48:49], s[42:43], 20
	s_and_b32 s79, s42, s78
	s_lshl_b32 s80, s25, 2
	s_and_b64 s[42:43], s[36:37], exec
	s_cselect_b32 s25, 0x800, 0
	s_add_u32 s82, s27, s48
	s_addc_u32 s83, s28, s49
	s_add_i32 s42, s79, s77
	s_lshl_b32 s42, s42, 9
	s_add_u32 s48, s82, s42
	s_addc_u32 s49, s83, 0
	s_add_u32 s50, s48, 0x10000
	s_addc_u32 s51, s49, 0
	s_add_u32 s52, s48, 0x40000
	s_addc_u32 s53, s49, 0
	s_add_u32 s54, s52, 0x10000
	s_addc_u32 s55, s53, 0
	s_add_u32 s58, s48, 0x80000
	s_addc_u32 s59, s49, 0
	s_add_u32 s60, s58, 0x10000
	s_addc_u32 s61, s59, 0
	s_and_b64 s[42:43], s[36:37], exec
	s_cselect_b32 s84, 0x200, 0
	v_add_u32_e32 v0, s25, v236
	s_mov_b32 s44, 0
	s_add_i32 s86, s84, s33
	v_add_u32_e32 v238, 0xd800, v0
	s_branch .LBB0_1419

.LBB0_1419:
	s_sub_i32 s56, s76, s44
	s_cmpk_lt_i32 s56, 0x241
	s_cselect_b64 s[42:43], -1, 0
	s_and_b64 s[62:63], s[36:37], s[42:43]
	s_mov_b64 s[42:43], -1
	s_and_b64 vcc, exec, s[62:63]
	s_cbranch_vccnz .LBB0_1418
	s_cmp_lg_u32 s44, 0
	s_cbranch_scc1 .Ldf_slow
	v_mov_b32_e32 v0, v231
	v_mov_b32_e32 v3, 0x24000
	v_cmp_gt_i32_e32 vcc, s76, v0
	v_add_u32_e32 v4, 0x200, v0
	s_nop 0
	v_cndmask_b32_e32 v2, v3, v216, vcc
	v_cmp_gt_i32_e32 vcc, s76, v4
	s_nop 1
	v_cndmask_b32_e32 v218, v3, v217, vcc
	s_branch .Ldf_b2
.Ldf_slow:
	v_mov_b32_e32 v0, v231
	v_mov_b32_e32 v2, 0x24000
	v_mov_b32_e32 v218, 0x24000
	v_add_u32_e32 v4, s44, v0
	v_cmp_gt_i32_e32 vcc, s76, v4
	s_and_saveexec_b64 s[42:43], vcc
	s_cbranch_execz .Ldf_a
	v_ashrrev_i32_e32 v5, 31, v4
	v_lshl_add_u64 v[4:5], v[4:5], 2, s[46:47]
	global_load_dword v2, v[4:5], off

.Ldf_b2:
	s_mov_b32 s25, 0x20000
	v_lshl_add_u32 v0, v0, 2, 0
	v_mov_b32_e32 v3, 0
	v_mov_b32_e32 v219, 0
	s_waitcnt vmcnt(0)
	ds_write_b32 v0, v2 offset:55296
	ds_write_b32 v0, v218 offset:57344
	v_cmp_gt_i32_e32 vcc, s25, v2
	s_and_saveexec_b64 s[42:43], vcc
	s_cbranch_execz .Ldf_c
	v_mov_b32_e32 v4, v2
	v_ashrrev_i32_e32 v5, 31, v2
	v_lshl_add_u64 v[4:5], v[4:5], 2, s[18:19]
	global_load_dword v3, v[4:5], off
